# v77 variant: chunk barrier 3 moved below the v-tile conversion VALU so the STL ds_write_b16 drain overlaps it
# baseline (speedup 1.0000x reference)
; #define LAS __attribute__((address_space(3)))
; #define LDS_BARRIER() do { asm volatile("s_waitcnt lgkmcnt(0)" ::: "memory"); __builtin_amdgcn_s_barrier(); asm volatile("" ::: "memory"); } while (0)
; template <int NET> __device__ __forceinline__ void ret_item(Ctx& F, int item) {
;     ...
;     for (int n = 0; n < 16; ++n) {
;         const int t0 = b * SEQ + n * 128;
;         RET_LOAD(n + 1 < 16 ? n + 1 : 15);
;         LDS_BARRIER();
;         f32x4 sacc[8];
; #pragma unroll
;         for (int mt = 0; mt < 8; ++mt) sacc[mt] = (f32x4){0.f, 0.f, 0.f, 0.f};
; #pragma unroll
;         for (int ks = 0; ks < 4; ++ks) { const bf16x8 bq = *(const LAS bf16x8*)(qL + (16 * w + fr) * LP + 32 * ks + 8 * fq);
; #pragma unroll
;             for (int mt = 0; mt < 8; ++mt) { const bf16x8 ak = *(const LAS bf16x8*)(kL + (16 * mt + fr) * LP + 32 * ks + 8 * fq); sacc[mt] = __builtin_amdgcn_mfma_f32_16x16x32_bf16(ak, bq, sacc[mt], 0, 0, 0); } }
.LBB0_314:
	s_add_i32 s74, s33, 0x80
	s_cmpk_eq_i32 s33, 0x780
	s_cselect_b32 s0, s33, s74
	v_add_u32_e32 v18, s0, v112
	v_mov_b64_e32 v[20:21], s[88:89]
	v_ashrrev_i32_e32 v19, 31, v18
	v_mad_i64_i32 v[20:21], s[0:1], v18, s91, v[20:21]
	v_lshlrev_b64 v[42:43], 8, v[18:19]
	v_lshl_add_u64 v[18:19], v[20:21], 0, v[106:107]
	global_load_dwordx4 v[26:29], v[18:19], off offset:16
	global_load_dwordx4 v[50:53], v[18:19], off
	global_load_dwordx4 v[30:33], v[18:19], off offset:144
	global_load_dwordx4 v[54:57], v[18:19], off offset:128
	global_load_dwordx4 v[34:37], v[18:19], off offset:2064
	global_load_dwordx4 v[58:61], v[18:19], off offset:2048
	global_load_dwordx4 v[38:41], v[18:19], off offset:2192
	global_load_dwordx4 v[62:65], v[18:19], off offset:2176
	v_lshl_add_u64 v[18:19], s[80:81], 1, v[20:21]
	v_lshl_add_u64 v[18:19], v[18:19], 0, v[106:107]
	v_lshl_add_u64 v[20:21], v[18:19], 0, s[78:79]
	v_add_co_u32_e64 v18, s[0:1], s92, v18
	v_lshl_add_u64 v[70:71], v[108:109], 0, v[42:43]
	s_nop 0
	v_addc_co_u32_e64 v19, s[0:1], 0, v19, s[0:1]
	global_load_dwordx4 v[22:25], v[18:19], off
	s_nop 0
	global_load_dwordx4 v[18:21], v[20:21], off offset:16
	s_nop 0
	global_load_dwordx4 v[42:45], v[70:71], off offset:48
	global_load_dwordx4 v[46:49], v[70:71], off offset:32
	global_load_dwordx4 v[66:69], v[70:71], off offset:16
	s_nop 0
	global_load_dwordx4 v[70:73], v[70:71], off
	s_waitcnt lgkmcnt(0)
	s_barrier
	ds_read_b128 v[74:77], v163
	ds_read_b128 v[78:81], v187 offset:34816
	ds_read_b128 v[82:85], v187 offset:39168
	ds_read_b128 v[86:89], v187 offset:43520
	ds_read_b128 v[90:93], v187 offset:47872
	ds_read_b128 v[94:97], v187 offset:52224
	ds_read_b128 v[98:101], v187 offset:56576
	ds_read_b128 v[102:105], v187 offset:60928
	ds_read_b128 v[232:235], v187 offset:65280
	s_waitcnt lgkmcnt(7)
	v_mfma_f32_16x16x32_bf16 v[78:81], v[78:81], v[74:77], 0
	v_add_u32_e32 v115, 0x1200, v166
	v_add_u32_e32 v130, 0x2400, v166
	v_add_u32_e32 v131, 0x3600, v166
	s_waitcnt lgkmcnt(6)
	v_mfma_f32_16x16x32_bf16 v[82:85], v[82:85], v[74:77], 0
	v_add_u32_e32 v132, 0x900, v166
	v_add_u32_e32 v133, 0x1b00, v166
	v_add_u32_e32 v248, 0x2d00, v166
	s_waitcnt lgkmcnt(5)
	v_mfma_f32_16x16x32_bf16 v[86:89], v[86:89], v[74:77], 0
	v_add_u32_e32 v249, 0x3f00, v166
	v_add_u32_e32 v124, s33, v111
	v_ashrrev_i32_e32 v125, 31, v124
	s_waitcnt lgkmcnt(4)
	v_mfma_f32_16x16x32_bf16 v[90:93], v[90:93], v[74:77], 0
	v_lshlrev_b64 v[124:125], 12, v[124:125]
	v_lshl_add_u64 v[124:125], v[120:121], 0, v[124:125]
	v_pk_mul_f32 v[10:11], v[122:123], v[10:11]
	s_waitcnt lgkmcnt(3)
	v_mfma_f32_16x16x32_bf16 v[94:97], v[94:97], v[74:77], 0
	v_mul_f32_e64 v14, v122, v14
	v_mul_f32_e64 v15, v123, v15
	v_pk_mul_f32 v[6:7], v[122:123], v[6:7]
	v_pk_mul_f32 v[2:3], v[122:123], v[2:3]
	s_waitcnt lgkmcnt(2)
	v_mfma_f32_16x16x32_bf16 v[98:101], v[98:101], v[74:77], 0
	s_cmpk_lg_i32 s74, 0x800
	s_mov_b32 s33, s74
	s_waitcnt lgkmcnt(1)
	v_mfma_f32_16x16x32_bf16 v[102:105], v[102:105], v[74:77], 0
	s_waitcnt lgkmcnt(0)
	v_mfma_f32_16x16x32_bf16 v[74:77], v[232:235], v[74:77], 0
	ds_read_b128 v[232:235], v163 offset:64
	ds_read_b128 v[236:239], v187 offset:34880
	s_waitcnt lgkmcnt(0)
	v_mfma_f32_16x16x32_bf16 v[78:81], v[236:239], v[232:235], v[78:81]
	ds_read_b128 v[236:239], v187 offset:39232
	s_waitcnt lgkmcnt(0)
	v_mfma_f32_16x16x32_bf16 v[82:85], v[236:239], v[232:235], v[82:85]
	ds_read_b128 v[236:239], v187 offset:43584
	s_waitcnt lgkmcnt(0)
	v_mfma_f32_16x16x32_bf16 v[86:89], v[236:239], v[232:235], v[86:89]
	ds_read_b128 v[236:239], v187 offset:47936
	s_waitcnt lgkmcnt(0)
	v_mfma_f32_16x16x32_bf16 v[90:93], v[236:239], v[232:235], v[90:93]
	ds_read_b128 v[236:239], v187 offset:52288
	s_waitcnt lgkmcnt(0)
	v_mfma_f32_16x16x32_bf16 v[94:97], v[236:239], v[232:235], v[94:97]
	ds_read_b128 v[236:239], v187 offset:56640
	s_waitcnt lgkmcnt(0)
	v_mfma_f32_16x16x32_bf16 v[98:101], v[236:239], v[232:235], v[98:101]
	ds_read_b128 v[236:239], v187 offset:60992
	s_waitcnt lgkmcnt(0)
	v_mfma_f32_16x16x32_bf16 v[102:105], v[236:239], v[232:235], v[102:105]
	ds_read_b128 v[236:239], v187 offset:65344
	s_waitcnt lgkmcnt(0)
	v_mfma_f32_16x16x32_bf16 v[74:77], v[236:239], v[232:235], v[74:77]
	ds_read_b128 v[232:235], v163 offset:128
	ds_read_b128 v[236:239], v187 offset:34944
	s_waitcnt lgkmcnt(0)
	v_mfma_f32_16x16x32_bf16 v[78:81], v[236:239], v[232:235], v[78:81]
	ds_read_b128 v[236:239], v187 offset:39296
	s_waitcnt lgkmcnt(0)
	v_mfma_f32_16x16x32_bf16 v[82:85], v[236:239], v[232:235], v[82:85]
	ds_read_b128 v[236:239], v187 offset:43648
	s_waitcnt lgkmcnt(0)
	v_mfma_f32_16x16x32_bf16 v[86:89], v[236:239], v[232:235], v[86:89]
	ds_read_b128 v[236:239], v187 offset:48000
	s_waitcnt lgkmcnt(0)
	v_mfma_f32_16x16x32_bf16 v[90:93], v[236:239], v[232:235], v[90:93]
	ds_read_b128 v[236:239], v187 offset:52352
	s_waitcnt lgkmcnt(0)
	v_mfma_f32_16x16x32_bf16 v[94:97], v[236:239], v[232:235], v[94:97]
	ds_read_b128 v[236:239], v187 offset:56704
	s_waitcnt lgkmcnt(0)
	v_mfma_f32_16x16x32_bf16 v[98:101], v[236:239], v[232:235], v[98:101]
	ds_read_b128 v[236:239], v187 offset:61056
	s_waitcnt lgkmcnt(0)
	v_mfma_f32_16x16x32_bf16 v[102:105], v[236:239], v[232:235], v[102:105]
	ds_read_b128 v[236:239], v187 offset:65408
	s_waitcnt lgkmcnt(0)
	v_mfma_f32_16x16x32_bf16 v[74:77], v[236:239], v[232:235], v[74:77]
	ds_read_b128 v[232:235], v163 offset:192
	ds_read_b128 v[236:239], v187 offset:35008
	s_waitcnt lgkmcnt(0)
	v_mfma_f32_16x16x32_bf16 v[78:81], v[236:239], v[232:235], v[78:81]
	ds_read_b128 v[236:239], v187 offset:39360
	s_waitcnt lgkmcnt(0)
; #define LAS __attribute__((address_space(3)))
; __device__ __forceinline__ unsigned pk2(float lo, float hi) { unsigned r; asm volatile("v_cvt_pk_bf16_f32 %0, %1, %2" : "=v"(r) : "v"(lo), "v"(hi)); return r; }
; template <int NET> __device__ __forceinline__ void ret_item(Ctx& F, int item) {
;     ...
;         for (int ks = 0; ks < 4; ++ks) { const bf16x8 bq = *(const LAS bf16x8*)(qL + (16 * w + fr) * LP + 32 * ks + 8 * fq);
; #pragma unroll
;             for (int mt = 0; mt < 8; ++mt) { const bf16x8 ak = *(const LAS bf16x8*)(kL + (16 * mt + fr) * LP + 32 * ks + 8 * fq); sacc[mt] = __builtin_amdgcn_mfma_f32_16x16x32_bf16(ak, bq, sacc[mt], 0, 0, 0); } }
;         const int c = 16 * w + fr;
;         bf16x8 pb[4];
; #pragma unroll
;         for (int sk = 0; sk < 4; ++sk) { unsigned pw[4];
; #pragma unroll
;             for (int hlf = 0; hlf < 2; ++hlf) { const int mt = 2 * sk + hlf; float pv[4];
; #pragma unroll
;                 for (int rr = 0; rr < 4; ++rr) { const int m = 16 * mt + 4 * fq + rr; pv[rr] = (c >= m) ? sacc[mt][rr] * dcm[mt][rr] : 0.f; }
;                 pw[2 * hlf] = pk2(pv[0], pv[1]); pw[2 * hlf + 1] = pk2(pv[2], pv[3]); }
;             pb[sk] = __builtin_bit_cast(bf16x8, (u32x4){pw[0], pw[1], pw[2], pw[3]}); }
;         { bf16x8 bqf[4];
; #pragma unroll
;           for (int ks = 0; ks < 4; ++ks) bqf[ks] = *(const LAS bf16x8*)(qL + (16 * w + fr) * LP + 32 * ks + 8 * fq);
;           const float qd = __builtin_amdgcn_exp2f(lg2 * (float)(c + 1));
; #pragma unroll
;           for (int et = 0; et < NET; ++et) { f32x4 oi = (f32x4){0.f, 0.f, 0.f, 0.f}, oc = (f32x4){0.f, 0.f, 0.f, 0.f};
;             bf16x8 avq[4]; const unsigned a0 = vLb + (unsigned)((4 * fq) * (VP * 2) + 32 * et); tr_quad(avq, a0, a0 + 32 * (VP * 2), a0 + 64 * (VP * 2), a0 + 96 * (VP * 2), 16 * (VP * 2));
; #pragma unroll
;             for (int ks = 0; ks < 4; ++ks) { const bf16x8 as = *(const LAS bf16x8*)(STL + (16 * et + fr) * LP + 32 * ks + 8 * fq);
;                 oi = __builtin_amdgcn_mfma_f32_16x16x32_bf16(avq[ks], pb[ks], oi, 0, 0, 0); oc = __builtin_amdgcn_mfma_f32_16x16x32_bf16(as, bqf[ks], oc, 0, 0, 0); }
;             *(f32x4*)(reto + (size_t)(t0 + c) * RW + h * 128 + eb * EW + 16 * et + 4 * fq) = oi + oc * qd; } }
	v_mfma_f32_16x16x32_bf16 v[82:85], v[236:239], v[232:235], v[82:85]
	ds_read_b128 v[236:239], v187 offset:43712
	s_waitcnt lgkmcnt(0)
	v_mfma_f32_16x16x32_bf16 v[86:89], v[236:239], v[232:235], v[86:89]
	ds_read_b128 v[236:239], v187 offset:48064
	s_waitcnt lgkmcnt(0)
	v_mfma_f32_16x16x32_bf16 v[90:93], v[236:239], v[232:235], v[90:93]
	ds_read_b128 v[236:239], v187 offset:52416
	s_waitcnt lgkmcnt(0)
	v_mfma_f32_16x16x32_bf16 v[94:97], v[236:239], v[232:235], v[94:97]
	ds_read_b128 v[236:239], v187 offset:56768
	s_waitcnt lgkmcnt(0)
	v_mfma_f32_16x16x32_bf16 v[98:101], v[236:239], v[232:235], v[98:101]
	ds_read_b128 v[236:239], v187 offset:61120
	s_waitcnt lgkmcnt(0)
	v_mfma_f32_16x16x32_bf16 v[102:105], v[236:239], v[232:235], v[102:105]
	ds_read_b128 v[236:239], v187 offset:65472
	s_waitcnt lgkmcnt(0)
	v_mfma_f32_16x16x32_bf16 v[232:235], v[236:239], v[232:235], v[74:77]
	s_nop 2
	v_mul_f32_e32 v74, v196, v78
	v_mul_f32_e32 v75, v197, v79
	v_mul_f32_e32 v76, v198, v80
	v_mul_f32_e32 v77, v199, v81
	v_cndmask_b32_e64 v74, v74, 0, vcc
	v_cndmask_b32_e64 v75, 0, v75, s[66:67]
	v_cndmask_b32_e64 v76, v76, 0, s[4:5]
	v_cndmask_b32_e64 v77, v77, 0, s[6:7]
	v_cvt_pk_bf16_f32 v74, v74, v75
	v_cvt_pk_bf16_f32 v75, v76, v77
	v_mul_f32_e32 v76, v200, v82
	v_mul_f32_e32 v77, v201, v83
	v_mul_f32_e32 v78, v202, v84
	v_mul_f32_e32 v79, v203, v85
	v_cndmask_b32_e64 v76, v76, 0, s[8:9]
	v_cndmask_b32_e64 v77, v77, 0, s[10:11]
	v_cndmask_b32_e64 v78, v78, 0, s[12:13]
	v_cndmask_b32_e64 v79, v79, 0, s[14:15]
	v_cvt_pk_bf16_f32 v76, v76, v77
	v_cvt_pk_bf16_f32 v77, v78, v79
	v_mul_f32_e32 v78, v204, v86
	v_mul_f32_e32 v79, v205, v87
	v_mul_f32_e32 v80, v206, v88
	v_mul_f32_e32 v81, v207, v89
	v_cndmask_b32_e64 v78, v78, 0, s[16:17]
	v_cndmask_b32_e64 v79, v79, 0, s[18:19]
	v_cndmask_b32_e64 v80, v80, 0, s[20:21]
	v_cndmask_b32_e64 v81, v81, 0, s[22:23]
	v_cvt_pk_bf16_f32 v78, v78, v79
	v_cvt_pk_bf16_f32 v79, v80, v81
	v_mul_f32_e32 v80, v208, v90
	v_mul_f32_e32 v81, v209, v91
	v_mul_f32_e32 v82, v210, v92
	v_mul_f32_e32 v83, v211, v93
	v_cndmask_b32_e64 v80, v80, 0, s[24:25]
	v_cndmask_b32_e64 v81, v81, 0, s[26:27]
	v_cndmask_b32_e64 v82, v82, 0, s[28:29]
	v_cndmask_b32_e64 v83, v83, 0, s[30:31]
	v_cvt_pk_bf16_f32 v80, v80, v81
	v_cvt_pk_bf16_f32 v81, v82, v83
	v_mul_f32_e32 v82, v212, v94
	v_mul_f32_e32 v83, v213, v95
	v_mul_f32_e32 v84, v214, v96
	v_mul_f32_e32 v85, v215, v97
	v_cndmask_b32_e64 v82, v82, 0, s[34:35]
	v_cndmask_b32_e64 v83, v83, 0, s[36:37]
	v_cndmask_b32_e64 v84, v84, 0, s[38:39]
	v_cndmask_b32_e64 v85, v85, 0, s[40:41]
	v_cvt_pk_bf16_f32 v82, v82, v83
	v_cvt_pk_bf16_f32 v83, v84, v85
	v_mul_f32_e32 v84, v216, v98
	v_mul_f32_e32 v85, v217, v99
	v_mul_f32_e32 v86, v218, v100
	v_mul_f32_e32 v87, v219, v101
	v_cndmask_b32_e64 v84, v84, 0, s[42:43]
	v_cndmask_b32_e64 v85, v85, 0, s[44:45]
	v_cndmask_b32_e64 v86, v86, 0, s[46:47]
	v_cndmask_b32_e64 v87, v87, 0, s[48:49]
	v_cvt_pk_bf16_f32 v84, v84, v85
	v_cvt_pk_bf16_f32 v85, v86, v87
	v_mul_f32_e32 v86, v220, v102
	v_mul_f32_e32 v87, v221, v103
	v_mul_f32_e32 v88, v222, v104
	v_mul_f32_e32 v89, v223, v105
	v_cndmask_b32_e64 v86, v86, 0, s[50:51]
	v_cndmask_b32_e64 v87, v87, 0, s[52:53]
	v_cndmask_b32_e64 v88, v88, 0, s[54:55]
	v_cndmask_b32_e64 v89, v89, 0, s[56:57]
	v_cvt_pk_bf16_f32 v86, v86, v87
	v_cvt_pk_bf16_f32 v87, v88, v89
	v_mul_f32_e32 v88, v224, v232
	v_mul_f32_e32 v89, v225, v233
	v_mul_f32_e32 v90, v226, v234
	v_cndmask_b32_e64 v88, v88, 0, s[58:59]
	v_cndmask_b32_e64 v89, v89, 0, s[60:61]
	v_cndmask_b32_e64 v90, v90, 0, s[62:63]
	v_mul_f32_e32 v91, v113, v235
	v_cndmask_b32_e64 v91, v91, 0, s[64:65]
	v_cvt_pk_bf16_f32 v88, v88, v89
	v_cvt_pk_bf16_f32 v89, v90, v91
	v_add_u32_e32 v90, v162, v164
	ds_read_b128 v[102:105], v90
	ds_read_b128 v[98:101], v90 offset:64
	ds_read_b128 v[94:97], v90 offset:128
	ds_read_b128 v[90:93], v90 offset:192
	ds_read_b64_tr_b16 v[244:245], v166
	ds_read_b64_tr_b16 v[246:247], v132
	ds_read_b64_tr_b16 v[240:241], v115
	ds_read_b64_tr_b16 v[242:243], v133
	ds_read_b64_tr_b16 v[236:237], v130
	ds_read_b64_tr_b16 v[238:239], v248
	ds_read_b64_tr_b16 v[232:233], v131
	ds_read_b64_tr_b16 v[234:235], v249
	s_waitcnt lgkmcnt(0)
	ds_read_b128 v[248:251], v188
	ds_read_b128 v[130:133], v188 offset:64
	v_mfma_f32_16x16x32_bf16 v[244:247], v[244:247], v[74:77], 0
	v_add_u32_e32 v115, 32, v166
	v_mfma_f32_16x16x32_bf16 v[240:243], v[240:243], v[78:81], v[244:247]
	s_waitcnt lgkmcnt(1)
	v_mfma_f32_16x16x32_bf16 v[248:251], v[248:251], v[102:105], 0
	s_nop 3
	ds_read_b128 v[244:247], v188 offset:128
	v_mfma_f32_16x16x32_bf16 v[236:239], v[236:239], v[82:85], v[240:243]
	s_nop 2
	ds_read_b128 v[240:243], v188 offset:192
	s_waitcnt lgkmcnt(2)
	v_mfma_f32_16x16x32_bf16 v[130:133], v[130:133], v[98:101], v[248:251]
	s_waitcnt lgkmcnt(1)
	v_mfma_f32_16x16x32_bf16 v[130:133], v[244:247], v[94:97], v[130:133]
	v_add_u32_e32 v244, 0x1220, v166
	v_add_u32_e32 v245, 0x2420, v166
	v_add_u32_e32 v246, 0x3620, v166
	v_mfma_f32_16x16x32_bf16 v[232:235], v[232:235], v[86:89], v[236:239]
	v_add_u32_e32 v247, 0x920, v166
	v_add_u32_e32 v248, 0x1b20, v166
	v_add_u32_e32 v249, 0x2d20, v166
	s_waitcnt lgkmcnt(0)
	v_mfma_f32_16x16x32_bf16 v[130:133], v[240:243], v[90:93], v[130:133]
	v_add_u32_e32 v250, 0x3f20, v166
	s_nop 6
	v_pk_fma_f32 v[132:133], v[118:119], v[132:133], v[234:235]
	v_pk_fma_f32 v[130:131], v[116:117], v[130:131], v[232:233]
	global_store_dwordx4 v[124:125], v[130:133], off
	s_nop 1
	ds_read_b64_tr_b16 v[240:241], v115
	ds_read_b64_tr_b16 v[242:243], v247
	ds_read_b64_tr_b16 v[236:237], v244
	ds_read_b64_tr_b16 v[238:239], v248
	ds_read_b64_tr_b16 v[232:233], v245
	ds_read_b64_tr_b16 v[234:235], v249
	ds_read_b64_tr_b16 v[130:131], v246
	ds_read_b64_tr_b16 v[132:133], v250
	s_waitcnt lgkmcnt(0)
; #define LAS __attribute__((address_space(3)))
; #define LDS_BARRIER() do { asm volatile("s_waitcnt lgkmcnt(0)" ::: "memory"); __builtin_amdgcn_s_barrier(); asm volatile("" ::: "memory"); } while (0)
; template <int NET> __device__ __forceinline__ void ret_item(Ctx& F, int item) {
;     ...
;           for (int et = 0; et < NET; ++et) { f32x4 oi = (f32x4){0.f, 0.f, 0.f, 0.f}, oc = (f32x4){0.f, 0.f, 0.f, 0.f};
;             bf16x8 avq[4]; const unsigned a0 = vLb + (unsigned)((4 * fq) * (VP * 2) + 32 * et); tr_quad(avq, a0, a0 + 32 * (VP * 2), a0 + 64 * (VP * 2), a0 + 96 * (VP * 2), 16 * (VP * 2));
; #pragma unroll
;             for (int ks = 0; ks < 4; ++ks) { const bf16x8 as = *(const LAS bf16x8*)(STL + (16 * et + fr) * LP + 32 * ks + 8 * fq);
;                 oi = __builtin_amdgcn_mfma_f32_16x16x32_bf16(avq[ks], pb[ks], oi, 0, 0, 0); oc = __builtin_amdgcn_mfma_f32_16x16x32_bf16(as, bqf[ks], oc, 0, 0, 0); }
;             *(f32x4*)(reto + (size_t)(t0 + c) * RW + h * 128 + eb * EW + 16 * et + 4 * fq) = oi + oc * qd; } }
;         LDS_BARRIER();
; #pragma unroll
;         for (int et = 0; et < NET; ++et) st[et] = st[et] * dec;
;         { bf16x8 bkq[4];
;           { const unsigned k0 = kLb + (unsigned)((8 * fq) * (LP * 2)); tr_quad(bkq, k0, k0 + 32 * (LP * 2), k0 + 64 * (LP * 2), k0 + 96 * (LP * 2), 4 * (LP * 2)); }
	ds_read_b128 v[244:247], v188 offset:4352
	ds_read_b128 v[248:251], v188 offset:4416
	v_mfma_f32_16x16x32_bf16 v[240:243], v[240:243], v[74:77], 0
	v_add_u32_e32 v115, 64, v166
	s_waitcnt lgkmcnt(1)
	v_mfma_f32_16x16x32_bf16 v[244:247], v[244:247], v[102:105], 0
	v_mfma_f32_16x16x32_bf16 v[236:239], v[236:239], v[78:81], v[240:243]
	s_waitcnt lgkmcnt(0)
	v_mfma_f32_16x16x32_bf16 v[240:243], v[248:251], v[98:101], v[244:247]
	v_add_u32_e32 v248, 0x1b40, v166
	v_add_u32_e32 v249, 0x2d40, v166
	v_add_u32_e32 v250, 0x3f40, v166
	s_nop 1
	ds_read_b128 v[244:247], v188 offset:4480
	v_mfma_f32_16x16x32_bf16 v[232:235], v[232:235], v[82:85], v[236:239]
	s_waitcnt lgkmcnt(0)
	v_mfma_f32_16x16x32_bf16 v[236:239], v[244:247], v[94:97], v[240:243]
	s_nop 2
	ds_read_b128 v[240:243], v188 offset:4544
	v_add_u32_e32 v244, 0x1240, v166
	v_add_u32_e32 v245, 0x2440, v166
	v_mfma_f32_16x16x32_bf16 v[130:133], v[130:133], v[86:89], v[232:235]
	v_add_u32_e32 v246, 0x3640, v166
	v_add_u32_e32 v247, 0x940, v166
	s_waitcnt lgkmcnt(0)
	v_mfma_f32_16x16x32_bf16 v[232:235], v[240:243], v[90:93], v[236:239]
	s_nop 7
	v_pk_fma_f32 v[132:133], v[118:119], v[234:235], v[132:133]
	v_pk_fma_f32 v[130:131], v[116:117], v[232:233], v[130:131]
	global_store_dwordx4 v[124:125], v[130:133], off offset:64
	s_nop 1
	ds_read_b64_tr_b16 v[240:241], v115
	ds_read_b64_tr_b16 v[242:243], v247
	ds_read_b64_tr_b16 v[236:237], v244
	ds_read_b64_tr_b16 v[238:239], v248
	ds_read_b64_tr_b16 v[232:233], v245
	ds_read_b64_tr_b16 v[234:235], v249
	ds_read_b64_tr_b16 v[130:131], v246
	ds_read_b64_tr_b16 v[132:133], v250
	s_waitcnt lgkmcnt(0)
	ds_read_b128 v[244:247], v188 offset:8704
	ds_read_b128 v[248:251], v188 offset:8768
	v_mfma_f32_16x16x32_bf16 v[240:243], v[240:243], v[74:77], 0
	v_add_u32_e32 v115, 0x60, v166
	s_waitcnt lgkmcnt(1)
	v_mfma_f32_16x16x32_bf16 v[244:247], v[244:247], v[102:105], 0
	v_mfma_f32_16x16x32_bf16 v[236:239], v[236:239], v[78:81], v[240:243]
	s_waitcnt lgkmcnt(0)
	v_mfma_f32_16x16x32_bf16 v[240:243], v[248:251], v[98:101], v[244:247]
	v_add_u32_e32 v248, 0x1b60, v166
	v_add_u32_e32 v249, 0x2d60, v166
	v_add_u32_e32 v250, 0x3f60, v166
	s_nop 1
	ds_read_b128 v[244:247], v188 offset:8832
	v_mfma_f32_16x16x32_bf16 v[232:235], v[232:235], v[82:85], v[236:239]
	s_waitcnt lgkmcnt(0)
	v_mfma_f32_16x16x32_bf16 v[236:239], v[244:247], v[94:97], v[240:243]
	s_nop 2
	ds_read_b128 v[240:243], v188 offset:8896
	v_add_u32_e32 v244, 0x1260, v166
	v_add_u32_e32 v245, 0x2460, v166
	v_mfma_f32_16x16x32_bf16 v[130:133], v[130:133], v[86:89], v[232:235]
	v_add_u32_e32 v246, 0x3660, v166
	v_add_u32_e32 v247, 0x960, v166
	s_waitcnt lgkmcnt(0)
	v_mfma_f32_16x16x32_bf16 v[232:235], v[240:243], v[90:93], v[236:239]
	s_nop 7
	v_pk_fma_f32 v[132:133], v[118:119], v[234:235], v[132:133]
	v_pk_fma_f32 v[130:131], v[116:117], v[232:233], v[130:131]
	global_store_dwordx4 v[124:125], v[130:133], off offset:128
	s_nop 1
	ds_read_b64_tr_b16 v[240:241], v115
	ds_read_b64_tr_b16 v[242:243], v247
	ds_read_b64_tr_b16 v[236:237], v244
	ds_read_b64_tr_b16 v[238:239], v248
	ds_read_b64_tr_b16 v[232:233], v245
	ds_read_b64_tr_b16 v[234:235], v249
	ds_read_b64_tr_b16 v[130:131], v246
	ds_read_b64_tr_b16 v[132:133], v250
	s_waitcnt lgkmcnt(0)
	ds_read_b128 v[244:247], v188 offset:13056
	v_mfma_f32_16x16x32_bf16 v[74:77], v[240:243], v[74:77], 0
	ds_read_b128 v[240:243], v188 offset:13120
	v_mov_b32_e32 v115, v114
	v_pk_mul_f32 v[12:13], v[114:115], v[12:13]
	s_waitcnt lgkmcnt(1)
	v_mfma_f32_16x16x32_bf16 v[102:105], v[244:247], v[102:105], 0
	v_mul_f32_e64 v16, v114, v16
	v_mul_f32_e64 v17, v115, v17
	v_pk_mul_f32 v[8:9], v[114:115], v[8:9]
	v_pk_mul_f32 v[4:5], v[114:115], v[4:5]
	v_mfma_f32_16x16x32_bf16 v[74:77], v[236:239], v[78:81], v[74:77]
	v_add_u32_e32 v115, 0x1200, v168
	s_waitcnt lgkmcnt(0)
	v_mfma_f32_16x16x32_bf16 v[78:81], v[240:243], v[98:101], v[102:105]
	ds_read_b128 v[98:101], v188 offset:13184
	v_mfma_f32_16x16x32_bf16 v[74:77], v[232:235], v[82:85], v[74:77]
	ds_read_b128 v[82:85], v188 offset:13248
	v_add_u32_e32 v232, 0x3860, v168
	s_waitcnt lgkmcnt(1)
	v_mfma_f32_16x16x32_bf16 v[78:81], v[98:101], v[94:97], v[78:81]
	v_add_u32_e32 v94, 0x2640, v167
	v_add_u32_e32 v95, 0x4840, v167
	v_add_u32_e32 v96, 0x6a40, v167
	v_mfma_f32_16x16x32_bf16 v[74:77], v[130:133], v[86:89], v[74:77]
	v_add_u32_e32 v130, 0x240, v168
	v_add_u32_e32 v131, 0x1440, v168
	v_add_u32_e32 v132, 0x2640, v168
	s_waitcnt lgkmcnt(0)
	v_mfma_f32_16x16x32_bf16 v[78:81], v[82:85], v[90:93], v[78:81]
	v_add_u32_e32 v90, 0x2200, v167
	v_add_u32_e32 v91, 0x4400, v167
	v_add_u32_e32 v92, 0x6600, v167
	v_add_u32_e32 v93, 0x440, v167
	v_add_u32_e32 v133, 0x3840, v168
	s_nop 2
	v_pk_fma_f32 v[76:77], v[118:119], v[80:81], v[76:77]
	v_pk_fma_f32 v[74:75], v[116:117], v[78:79], v[74:75]
	global_store_dwordx4 v[124:125], v[74:77], off offset:192
	s_waitcnt lgkmcnt(0)
	s_barrier
; template <int NET> __device__ __forceinline__ void ret_item(Ctx& F, int item) {
;     ...
;             for (int hh = 0; hh < 2; ++hh) { unsigned oq1[4], oq2[4], ok1[4], ok2[4];
; #pragma unroll
;                 for (int c = 0; c < 4; ++c) { float a[2], bq[2], ka[2], kb[2];
; #pragma unroll
;                     for (int z = 0; z < 2; ++z) { const int jj = hh * 8 + c * 2 + z; const unsigned cw_ = cs4[jj >> 2][jj & 3]; const f32x2 sc = (f32x2){bflo(cw_), bfhi(cw_)};
;                         const float x1 = z ? bfhi(q1[hh][c]) : bflo(q1[hh][c]), x2 = z ? bfhi(q2[hh][c]) : bflo(q2[hh][c]);
;                         const float y1 = z ? bfhi(k1[hh][c]) : bflo(k1[hh][c]), y2 = z ? bfhi(k2[hh][c]) : bflo(k2[hh][c]);
;                         a[z] = (x1 * sc.x - x2 * sc.y) * 0.08838834764831845f; bq[z] = (x2 * sc.x + x1 * sc.y) * 0.08838834764831845f;
;                         ka[z] = y1 * sc.x - y2 * sc.y; kb[z] = y2 * sc.x + y1 * sc.y;
;                     }
;                     oq1[c] = pk2(a[0], a[1]); oq2[c] = pk2(bq[0], bq[1]); ok1[c] = pk2(ka[0], ka[1]); ok2[c] = pk2(kb[0], kb[1]); }
;                 *(LAS u32x4*)(qL + r * LP + j0 + hh * 8) = (u32x4){oq1[0], oq1[1], oq1[2], oq1[3]}; *(LAS u32x4*)(qL + r * LP + 64 + j0 + hh * 8) = (u32x4){oq2[0], oq2[1], oq2[2], oq2[3]};
;                 *(LAS u32x4*)(kL + r * LP + j0 + hh * 8) = (u32x4){ok1[0], ok1[1], ok1[2], ok1[3]}; *(LAS u32x4*)(kL + r * LP + 64 + j0 + hh * 8) = (u32x4){ok2[0], ok2[1], ok2[2], ok2[3]}; }
; #pragma unroll
;             for (int vi = 0; vi < NET / 2; ++vi) { unsigned vd[4];
; #pragma unroll
;     ...
;         { bf16x8 bkq[4];
;           { const unsigned k0 = kLb + (unsigned)((8 * fq) * (LP * 2)); tr_quad(bkq, k0, k0 + 32 * (LP * 2), k0 + 64 * (LP * 2), k0 + 96 * (LP * 2), 4 * (LP * 2)); }
; #pragma unroll
;           for (int et = 0; et < NET; ++et) { bf16x8 vq[4]; const unsigned v0 = vdLb + (unsigned)((8 * fq) * (VP * 2) + 32 * et); tr_quad(vq, v0, v0 + 32 * (VP * 2), v0 + 64 * (VP * 2), v0 + 96 * (VP * 2), 4 * (VP * 2));
; #pragma unroll
;             for (int ks = 0; ks < 4; ++ks) st[et] = __builtin_amdgcn_mfma_f32_16x16x32_bf16(vq[ks], bkq[ks], st[et], 0, 0, 0); } }
; #pragma unroll
;         for (int et = 0; et < NET; ++et)
; #pragma unroll
;             for (int rr = 0; rr < 4; ++rr) STL[(16 * et + 4 * fq + rr) * LP + 16 * w + fr] = f2bf(st[et][rr]);
;         LDS_BARRIER();
	v_add_u32_e32 v124, 0x2400, v168
	ds_read_b64_tr_b16 v[86:87], v167
	ds_read_b64_tr_b16 v[88:89], v93
	ds_read_b64_tr_b16 v[82:83], v90
	ds_read_b64_tr_b16 v[84:85], v94
	ds_read_b64_tr_b16 v[78:79], v91
	ds_read_b64_tr_b16 v[80:81], v95
	ds_read_b64_tr_b16 v[74:75], v92
	ds_read_b64_tr_b16 v[76:77], v96
	s_waitcnt lgkmcnt(0)
	v_add_u32_e32 v125, 0x3600, v168
	ds_read_b64_tr_b16 v[102:103], v168
	ds_read_b64_tr_b16 v[104:105], v130
	ds_read_b64_tr_b16 v[98:99], v115
	ds_read_b64_tr_b16 v[100:101], v131
	ds_read_b64_tr_b16 v[94:95], v124
	ds_read_b64_tr_b16 v[96:97], v132
	ds_read_b64_tr_b16 v[90:91], v125
	ds_read_b64_tr_b16 v[92:93], v133
	s_waitcnt lgkmcnt(0)
	v_add_u32_e32 v115, 32, v168
	v_mfma_f32_16x16x32_bf16 v[10:13], v[102:105], v[86:89], v[10:13]
	v_add_u32_e32 v124, 0x1220, v168
	v_add_u32_e32 v125, 0x2420, v168
	v_add_u32_e32 v130, 0x3620, v168
	v_mfma_f32_16x16x32_bf16 v[10:13], v[98:101], v[82:85], v[10:13]
	v_add_u32_e32 v131, 0x260, v168
	v_add_u32_e32 v132, 0x1460, v168
	v_add_u32_e32 v133, 0x2660, v168
	v_mfma_f32_16x16x32_bf16 v[10:13], v[94:97], v[78:81], v[10:13]
	v_mfma_f32_16x16x32_bf16 v[10:13], v[90:93], v[74:77], v[10:13]
	ds_read_b64_tr_b16 v[102:103], v115
	ds_read_b64_tr_b16 v[104:105], v131
	ds_read_b64_tr_b16 v[98:99], v124
	ds_read_b64_tr_b16 v[100:101], v132
	ds_read_b64_tr_b16 v[94:95], v125
	ds_read_b64_tr_b16 v[96:97], v133
	ds_read_b64_tr_b16 v[90:91], v130
	ds_read_b64_tr_b16 v[92:93], v232
	s_waitcnt lgkmcnt(0)
	v_add_u32_e32 v115, 64, v168
	v_mfma_f32_16x16x32_bf16 v[14:17], v[102:105], v[86:89], v[14:17]
	v_mfma_f32_16x16x32_bf16 v[14:17], v[98:101], v[82:85], v[14:17]
	v_mfma_f32_16x16x32_bf16 v[14:17], v[94:97], v[78:81], v[14:17]
	v_mfma_f32_16x16x32_bf16 v[14:17], v[90:93], v[74:77], v[14:17]
	ds_read_b64_tr_b16 v[102:103], v115
	ds_read_b64_tr_b16 v[104:105], v172
	ds_read_b64_tr_b16 v[98:99], v169
	ds_read_b64_tr_b16 v[100:101], v173
	ds_read_b64_tr_b16 v[94:95], v170
	ds_read_b64_tr_b16 v[96:97], v174
	ds_read_b64_tr_b16 v[90:91], v171
	ds_read_b64_tr_b16 v[92:93], v175
	s_waitcnt lgkmcnt(0)
	s_nop 0
	v_mfma_f32_16x16x32_bf16 v[6:9], v[102:105], v[86:89], v[6:9]
	v_mfma_f32_16x16x32_bf16 v[6:9], v[98:101], v[82:85], v[6:9]
	v_mfma_f32_16x16x32_bf16 v[6:9], v[94:97], v[78:81], v[6:9]
	v_mfma_f32_16x16x32_bf16 v[6:9], v[90:93], v[74:77], v[6:9]
	ds_read_b64_tr_b16 v[102:103], v176
	ds_read_b64_tr_b16 v[104:105], v180
	ds_read_b64_tr_b16 v[98:99], v177
	ds_read_b64_tr_b16 v[100:101], v181
	ds_read_b64_tr_b16 v[94:95], v178
	ds_read_b64_tr_b16 v[96:97], v182
	ds_read_b64_tr_b16 v[90:91], v179
	ds_read_b64_tr_b16 v[92:93], v183
	s_waitcnt lgkmcnt(0)
	s_nop 0
	v_mfma_f32_16x16x32_bf16 v[2:5], v[102:105], v[86:89], v[2:5]
	v_mfma_f32_16x16x32_bf16 v[2:5], v[98:101], v[82:85], v[2:5]
	v_mfma_f32_16x16x32_bf16 v[2:5], v[94:97], v[78:81], v[2:5]
	s_waitcnt vmcnt(14)
	v_lshlrev_b32_e32 v79, 16, v54
	v_lshlrev_b32_e32 v78, 16, v50
	v_mfma_f32_16x16x32_bf16 v[2:5], v[90:93], v[74:77], v[2:5]
	v_cvt_pk_bf16_f32 v74, v10, s0
	ds_write_b16 v189, v74
	v_cvt_pk_bf16_f32 v74, v11, s0
	ds_write_b16 v190, v74
	v_cvt_pk_bf16_f32 v74, v12, s0
	ds_write_b16 v190, v74 offset:272
	v_cvt_pk_bf16_f32 v74, v13, s0
	ds_write_b16 v190, v74 offset:544
	v_cvt_pk_bf16_f32 v74, v14, s0
	ds_write_b16 v190, v74 offset:4080
	v_cvt_pk_bf16_f32 v74, v15, s0
	ds_write_b16 v190, v74 offset:4352
	v_cvt_pk_bf16_f32 v74, v16, s0
	ds_write_b16 v190, v74 offset:4624
	v_cvt_pk_bf16_f32 v74, v17, s0
	ds_write_b16 v190, v74 offset:4896
	v_cvt_pk_bf16_f32 v74, v6, s0
	ds_write_b16 v190, v74 offset:8432
	v_cvt_pk_bf16_f32 v74, v7, s0
	ds_write_b16 v190, v74 offset:8704
	v_cvt_pk_bf16_f32 v74, v8, s0
	ds_write_b16 v190, v74 offset:8976
	v_cvt_pk_bf16_f32 v74, v9, s0
	ds_write_b16 v190, v74 offset:9248
	v_cvt_pk_bf16_f32 v74, v2, s0
	ds_write_b16 v190, v74 offset:12784
	v_cvt_pk_bf16_f32 v74, v3, s0
	ds_write_b16 v190, v74 offset:13056
	v_cvt_pk_bf16_f32 v74, v4, s0
	ds_write_b16 v190, v74 offset:13328
	v_cvt_pk_bf16_f32 v74, v5, s0
	ds_write_b16 v190, v74 offset:13600
	s_waitcnt vmcnt(4)
	v_and_b32_e32 v74, 0xffff0000, v70
	v_lshlrev_b32_e32 v75, 16, v70
	v_pk_mul_f32 v[80:81], v[74:75], v[78:79] op_sel:[1,0] op_sel_hi:[0,1]
	v_sub_f32_e32 v70, v80, v81
	v_pk_mul_f32 v[78:79], v[78:79], v[74:75]
	v_lshlrev_b32_e32 v77, 16, v62
	v_lshlrev_b32_e32 v76, 16, v58
	v_mul_f32_e32 v80, 0x3db504f3, v70
	v_add_f32_e32 v70, v78, v79
	v_mul_f32_e32 v81, 0x3db504f3, v70
	v_pk_mul_f32 v[78:79], v[74:75], v[76:77] op_sel:[1,0] op_sel_hi:[0,1]
	v_pk_mul_f32 v[74:75], v[76:77], v[74:75]
	v_and_b32_e32 v70, 0xffff0000, v71
	v_lshlrev_b32_e32 v71, 16, v71
	v_and_b32_e32 v77, 0xffff0000, v54
	v_and_b32_e32 v76, 0xffff0000, v50
	v_sub_f32_e32 v82, v78, v79
	v_add_f32_e32 v83, v74, v75
	v_and_b32_e32 v75, 0xffff0000, v62
	v_and_b32_e32 v74, 0xffff0000, v58
	v_pk_mul_f32 v[78:79], v[70:71], v[76:77] op_sel:[1,0] op_sel_hi:[0,1]
	v_pk_mul_f32 v[76:77], v[76:77], v[70:71]
	v_sub_f32_e32 v50, v78, v79
	v_add_f32_e32 v54, v76, v77
	v_pk_mul_f32 v[76:77], v[70:71], v[74:75] op_sel:[1,0] op_sel_hi:[0,1]
	v_pk_mul_f32 v[70:71], v[74:75], v[70:71]
	v_mul_f32_e32 v50, 0x3db504f3, v50
	v_mul_f32_e32 v54, 0x3db504f3, v54
	v_sub_f32_e32 v76, v76, v77
	v_add_f32_e32 v70, v70, v71
	v_lshlrev_b32_e32 v92, 16, v22
	v_and_b32_e32 v93, 0xffff0000, v22
	v_mul_f32_e32 v92, v227, v92
	v_mul_f32_e32 v93, v227, v93
	v_cvt_pk_bf16_f32 v84, v92, v93
	v_lshlrev_b32_e32 v92, 16, v23
	v_and_b32_e32 v93, 0xffff0000, v23
	v_mul_f32_e32 v92, v227, v92
	v_mul_f32_e32 v93, v227, v93
	v_cvt_pk_bf16_f32 v85, v92, v93
	v_lshlrev_b32_e32 v92, 16, v24
	v_and_b32_e32 v93, 0xffff0000, v24
	v_mul_f32_e32 v92, v227, v92
	v_mul_f32_e32 v93, v227, v93
	v_cvt_pk_bf16_f32 v86, v92, v93
	v_lshlrev_b32_e32 v92, 16, v25
	v_and_b32_e32 v93, 0xffff0000, v25
	v_mul_f32_e32 v92, v227, v92
	v_mul_f32_e32 v93, v227, v93
	v_cvt_pk_bf16_f32 v87, v92, v93
	v_lshlrev_b32_e32 v92, 16, v18
	v_and_b32_e32 v93, 0xffff0000, v18
	v_mul_f32_e32 v92, v227, v92
	v_mul_f32_e32 v93, v227, v93
	v_cvt_pk_bf16_f32 v88, v92, v93
	v_lshlrev_b32_e32 v92, 16, v19
	v_and_b32_e32 v93, 0xffff0000, v19
	v_mul_f32_e32 v92, v227, v92
	v_mul_f32_e32 v93, v227, v93
	v_cvt_pk_bf16_f32 v89, v92, v93
	v_lshlrev_b32_e32 v92, 16, v20
	v_and_b32_e32 v93, 0xffff0000, v20
	v_mul_f32_e32 v92, v227, v92
	v_mul_f32_e32 v93, v227, v93
	v_cvt_pk_bf16_f32 v90, v92, v93
	v_lshlrev_b32_e32 v92, 16, v21
	v_and_b32_e32 v93, 0xffff0000, v21
	v_mul_f32_e32 v92, v227, v92
	v_mul_f32_e32 v93, v227, v93
	v_cvt_pk_bf16_f32 v91, v92, v93
	s_waitcnt lgkmcnt(0)
	s_barrier
; #define LAS __attribute__((address_space(3)))
; __device__ __forceinline__ unsigned pk2(float lo, float hi) { unsigned r; asm volatile("v_cvt_pk_bf16_f32 %0, %1, %2" : "=v"(r) : "v"(lo), "v"(hi)); return r; }
; __device__ __forceinline__ float bflo(unsigned w) { return __uint_as_float(w << 16); }
; __device__ __forceinline__ float bfhi(unsigned w) { return __uint_as_float(w & 0xffff0000u); }
; template <int NET> __device__ __forceinline__ void ret_item(Ctx& F, int item) {
;     ...
;             for (int hh = 0; hh < 2; ++hh) { unsigned oq1[4], oq2[4], ok1[4], ok2[4];
; #pragma unroll
;                 for (int c = 0; c < 4; ++c) { float a[2], bq[2], ka[2], kb[2];
; #pragma unroll
;                     for (int z = 0; z < 2; ++z) { const int jj = hh * 8 + c * 2 + z; const unsigned cw_ = cs4[jj >> 2][jj & 3]; const f32x2 sc = (f32x2){bflo(cw_), bfhi(cw_)};
;                         const float x1 = z ? bfhi(q1[hh][c]) : bflo(q1[hh][c]), x2 = z ? bfhi(q2[hh][c]) : bflo(q2[hh][c]);
;                         const float y1 = z ? bfhi(k1[hh][c]) : bflo(k1[hh][c]), y2 = z ? bfhi(k2[hh][c]) : bflo(k2[hh][c]);
;                         a[z] = (x1 * sc.x - x2 * sc.y) * 0.08838834764831845f; bq[z] = (x2 * sc.x + x1 * sc.y) * 0.08838834764831845f;
;                         ka[z] = y1 * sc.x - y2 * sc.y; kb[z] = y2 * sc.x + y1 * sc.y;
;                     }
;                     oq1[c] = pk2(a[0], a[1]); oq2[c] = pk2(bq[0], bq[1]); ok1[c] = pk2(ka[0], ka[1]); ok2[c] = pk2(kb[0], kb[1]); }
;                 *(LAS u32x4*)(qL + r * LP + j0 + hh * 8) = (u32x4){oq1[0], oq1[1], oq1[2], oq1[3]}; *(LAS u32x4*)(qL + r * LP + 64 + j0 + hh * 8) = (u32x4){oq2[0], oq2[1], oq2[2], oq2[3]};
;                 *(LAS u32x4*)(kL + r * LP + j0 + hh * 8) = (u32x4){ok1[0], ok1[1], ok1[2], ok1[3]}; *(LAS u32x4*)(kL + r * LP + 64 + j0 + hh * 8) = (u32x4){ok2[0], ok2[1], ok2[2], ok2[3]}; }
; #pragma unroll
;             for (int vi = 0; vi < NET / 2; ++vi) { unsigned vd[4];
; #pragma unroll
;                 for (int c = 0; c < 4; ++c) vd[c] = pk2(bflo(vv[vi][c]) * kdec, bfhi(vv[vi][c]) * kdec);
;                 *(LAS u32x4*)(vL + r * VP + qd * (EW / 4) + 8 * vi) = vv[vi]; *(LAS u32x4*)(vdL + r * VP + qd * (EW / 4) + 8 * vi) = (u32x4){vd[0], vd[1], vd[2], vd[3]}; }
	ds_write_b128 v194, v[22:25]
	ds_write_b128 v195, v[84:87]
	ds_write_b128 v194, v[18:21] offset:16
	ds_write_b128 v195, v[88:91] offset:16
	v_cvt_pk_bf16_f32 v62, v80, v50
	v_cvt_pk_bf16_f32 v58, v81, v54
	v_cvt_pk_bf16_f32 v54, v82, v76
	v_cvt_pk_bf16_f32 v50, v83, v70
	v_and_b32_e32 v70, 0xffff0000, v72
	v_lshlrev_b32_e32 v71, 16, v72
	v_lshlrev_b32_e32 v77, 16, v55
	v_lshlrev_b32_e32 v76, 16, v51
	v_pk_mul_f32 v[78:79], v[70:71], v[76:77] op_sel:[1,0] op_sel_hi:[0,1]
	v_lshlrev_b32_e32 v75, 16, v63
	v_lshlrev_b32_e32 v74, 16, v59
	v_sub_f32_e32 v72, v78, v79
	v_pk_mul_f32 v[76:77], v[76:77], v[70:71]
	v_mul_f32_e32 v78, 0x3db504f3, v72
	v_add_f32_e32 v72, v76, v77
	v_pk_mul_f32 v[76:77], v[70:71], v[74:75] op_sel:[1,0] op_sel_hi:[0,1]
	v_pk_mul_f32 v[70:71], v[74:75], v[70:71]
	v_and_b32_e32 v75, 0xffff0000, v55
	v_add_f32_e32 v81, v70, v71
	v_and_b32_e32 v70, 0xffff0000, v73
	v_lshlrev_b32_e32 v71, 16, v73
	v_and_b32_e32 v74, 0xffff0000, v51
	v_mul_f32_e32 v79, 0x3db504f3, v72
	v_sub_f32_e32 v80, v76, v77
	v_and_b32_e32 v73, 0xffff0000, v63
	v_and_b32_e32 v72, 0xffff0000, v59
	v_pk_mul_f32 v[76:77], v[70:71], v[74:75] op_sel:[1,0] op_sel_hi:[0,1]
	v_pk_mul_f32 v[74:75], v[74:75], v[70:71]
	v_sub_f32_e32 v51, v76, v77
	v_add_f32_e32 v55, v74, v75
	v_pk_mul_f32 v[74:75], v[70:71], v[72:73] op_sel:[1,0] op_sel_hi:[0,1]
	v_pk_mul_f32 v[70:71], v[72:73], v[70:71]
	v_mul_f32_e32 v51, 0x3db504f3, v51
	v_mul_f32_e32 v55, 0x3db504f3, v55
	v_sub_f32_e32 v74, v74, v75
	v_add_f32_e32 v70, v70, v71
	v_cvt_pk_bf16_f32 v63, v78, v51
	v_cvt_pk_bf16_f32 v59, v79, v55
	v_cvt_pk_bf16_f32 v55, v80, v74
	v_cvt_pk_bf16_f32 v51, v81, v70
	v_and_b32_e32 v70, 0xffff0000, v66
	v_lshlrev_b32_e32 v71, 16, v66
	v_lshlrev_b32_e32 v75, 16, v56
	v_lshlrev_b32_e32 v74, 16, v52
	v_pk_mul_f32 v[76:77], v[70:71], v[74:75] op_sel:[1,0] op_sel_hi:[0,1]
	v_sub_f32_e32 v66, v76, v77
	v_pk_mul_f32 v[74:75], v[74:75], v[70:71]
	v_lshlrev_b32_e32 v73, 16, v64
	v_lshlrev_b32_e32 v72, 16, v60
	v_mul_f32_e32 v76, 0x3db504f3, v66
	v_add_f32_e32 v66, v74, v75
	v_mul_f32_e32 v77, 0x3db504f3, v66
	v_pk_mul_f32 v[74:75], v[70:71], v[72:73] op_sel:[1,0] op_sel_hi:[0,1]
	v_pk_mul_f32 v[70:71], v[72:73], v[70:71]
	v_and_b32_e32 v66, 0xffff0000, v67
	v_lshlrev_b32_e32 v67, 16, v67
	v_and_b32_e32 v73, 0xffff0000, v56
	v_and_b32_e32 v72, 0xffff0000, v52
	v_sub_f32_e32 v78, v74, v75
	v_add_f32_e32 v79, v70, v71
	v_and_b32_e32 v71, 0xffff0000, v64
	v_and_b32_e32 v70, 0xffff0000, v60
	v_pk_mul_f32 v[74:75], v[66:67], v[72:73] op_sel:[1,0] op_sel_hi:[0,1]
	v_pk_mul_f32 v[72:73], v[72:73], v[66:67]
	v_sub_f32_e32 v52, v74, v75
	v_add_f32_e32 v56, v72, v73
	v_pk_mul_f32 v[72:73], v[66:67], v[70:71] op_sel:[1,0] op_sel_hi:[0,1]
	v_pk_mul_f32 v[66:67], v[70:71], v[66:67]
	v_mul_f32_e32 v52, 0x3db504f3, v52
	v_mul_f32_e32 v56, 0x3db504f3, v56
	v_sub_f32_e32 v72, v72, v73
	v_add_f32_e32 v66, v66, v67
	v_cvt_pk_bf16_f32 v64, v76, v52
	v_cvt_pk_bf16_f32 v60, v77, v56
	v_cvt_pk_bf16_f32 v56, v78, v72
	v_cvt_pk_bf16_f32 v52, v79, v66
	v_and_b32_e32 v66, 0xffff0000, v68
	v_lshlrev_b32_e32 v67, 16, v68
	v_lshlrev_b32_e32 v73, 16, v57
	v_lshlrev_b32_e32 v72, 16, v53
	v_pk_mul_f32 v[74:75], v[66:67], v[72:73] op_sel:[1,0] op_sel_hi:[0,1]
	v_lshlrev_b32_e32 v71, 16, v65
	v_lshlrev_b32_e32 v70, 16, v61
	v_sub_f32_e32 v68, v74, v75
	v_pk_mul_f32 v[72:73], v[72:73], v[66:67]
	v_mul_f32_e32 v74, 0x3db504f3, v68
	v_add_f32_e32 v68, v72, v73
	v_pk_mul_f32 v[72:73], v[66:67], v[70:71] op_sel:[1,0] op_sel_hi:[0,1]
	v_pk_mul_f32 v[66:67], v[70:71], v[66:67]
	v_and_b32_e32 v71, 0xffff0000, v57
	v_add_f32_e32 v77, v66, v67
	v_and_b32_e32 v66, 0xffff0000, v69
	v_lshlrev_b32_e32 v67, 16, v69
	v_and_b32_e32 v70, 0xffff0000, v53
	v_sub_f32_e32 v76, v72, v73
	v_pk_mul_f32 v[72:73], v[66:67], v[70:71] op_sel:[1,0] op_sel_hi:[0,1]
	v_pk_mul_f32 v[70:71], v[70:71], v[66:67]
	v_mul_f32_e32 v75, 0x3db504f3, v68
	v_and_b32_e32 v69, 0xffff0000, v65
	v_and_b32_e32 v68, 0xffff0000, v61
	v_sub_f32_e32 v53, v72, v73
	v_add_f32_e32 v57, v70, v71
	v_mul_f32_e32 v53, 0x3db504f3, v53
	v_mul_f32_e32 v57, 0x3db504f3, v57
	v_pk_mul_f32 v[70:71], v[66:67], v[68:69] op_sel:[1,0] op_sel_hi:[0,1]
	v_pk_mul_f32 v[66:67], v[68:69], v[66:67]
	v_sub_f32_e32 v70, v70, v71
	v_add_f32_e32 v66, v66, v67
	v_cvt_pk_bf16_f32 v65, v74, v53
	v_cvt_pk_bf16_f32 v61, v75, v57
	v_cvt_pk_bf16_f32 v57, v76, v70
	v_cvt_pk_bf16_f32 v53, v77, v66
	ds_write_b128 v161, v[62:65]
	ds_write_b128 v161, v[58:61] offset:128
	ds_write_b128 v161, v[54:57] offset:34816
	ds_write_b128 v161, v[50:53] offset:34944
	v_lshlrev_b32_e32 v50, 16, v46
	v_and_b32_e32 v51, 0xffff0000, v46
	v_lshlrev_b32_e32 v53, 16, v30
	v_lshlrev_b32_e32 v52, 16, v26
	v_pk_mul_f32 v[54:55], v[52:53], v[50:51]
	v_pk_mul_f32 v[52:53], v[50:51], v[52:53] op_sel:[1,0] op_sel_hi:[0,1]
	v_sub_f32_e32 v46, v54, v55
	v_mul_f32_e32 v56, 0x3db504f3, v46
	v_add_f32_e32 v46, v52, v53
	v_lshlrev_b32_e32 v53, 16, v38
	v_lshlrev_b32_e32 v52, 16, v34
	v_pk_mul_f32 v[54:55], v[52:53], v[50:51]
	v_pk_mul_f32 v[50:51], v[50:51], v[52:53] op_sel:[1,0] op_sel_hi:[0,1]
	v_mul_f32_e32 v57, 0x3db504f3, v46
	v_sub_f32_e32 v54, v54, v55
	v_add_f32_e32 v55, v50, v51
; #define LAS __attribute__((address_space(3)))
; __device__ __forceinline__ unsigned pk2(float lo, float hi) { unsigned r; asm volatile("v_cvt_pk_bf16_f32 %0, %1, %2" : "=v"(r) : "v"(lo), "v"(hi)); return r; }
; __device__ __forceinline__ float bflo(unsigned w) { return __uint_as_float(w << 16); }
; __device__ __forceinline__ float bfhi(unsigned w) { return __uint_as_float(w & 0xffff0000u); }
; template <int NET> __device__ __forceinline__ void ret_item(Ctx& F, int item) {
;     ...
;             for (int hh = 0; hh < 2; ++hh) { unsigned oq1[4], oq2[4], ok1[4], ok2[4];
; #pragma unroll
;                 for (int c = 0; c < 4; ++c) { float a[2], bq[2], ka[2], kb[2];
; #pragma unroll
;                     for (int z = 0; z < 2; ++z) { const int jj = hh * 8 + c * 2 + z; const unsigned cw_ = cs4[jj >> 2][jj & 3]; const f32x2 sc = (f32x2){bflo(cw_), bfhi(cw_)};
;                         const float x1 = z ? bfhi(q1[hh][c]) : bflo(q1[hh][c]), x2 = z ? bfhi(q2[hh][c]) : bflo(q2[hh][c]);
;                         const float y1 = z ? bfhi(k1[hh][c]) : bflo(k1[hh][c]), y2 = z ? bfhi(k2[hh][c]) : bflo(k2[hh][c]);
;                         a[z] = (x1 * sc.x - x2 * sc.y) * 0.08838834764831845f; bq[z] = (x2 * sc.x + x1 * sc.y) * 0.08838834764831845f;
;                         ka[z] = y1 * sc.x - y2 * sc.y; kb[z] = y2 * sc.x + y1 * sc.y;
;                     }
;                     oq1[c] = pk2(a[0], a[1]); oq2[c] = pk2(bq[0], bq[1]); ok1[c] = pk2(ka[0], ka[1]); ok2[c] = pk2(kb[0], kb[1]); }
;                 *(LAS u32x4*)(qL + r * LP + j0 + hh * 8) = (u32x4){oq1[0], oq1[1], oq1[2], oq1[3]}; *(LAS u32x4*)(qL + r * LP + 64 + j0 + hh * 8) = (u32x4){oq2[0], oq2[1], oq2[2], oq2[3]};
;                 *(LAS u32x4*)(kL + r * LP + j0 + hh * 8) = (u32x4){ok1[0], ok1[1], ok1[2], ok1[3]}; *(LAS u32x4*)(kL + r * LP + 64 + j0 + hh * 8) = (u32x4){ok2[0], ok2[1], ok2[2], ok2[3]}; }
; __global__ void __launch_bounds__(NWAVES * 64, 2) fwd_kernel(Args args) {
;     ...
;             if (!split || (F.vcu & 1) == 0) { for (int it = hw; it < NB * 8 * 2; it += HS) ret_item<4>(F, it); }
	v_lshlrev_b32_e32 v46, 16, v47
	v_and_b32_e32 v47, 0xffff0000, v47
	v_and_b32_e32 v51, 0xffff0000, v30
	v_and_b32_e32 v50, 0xffff0000, v26
	v_pk_mul_f32 v[52:53], v[50:51], v[46:47]
	v_pk_mul_f32 v[50:51], v[46:47], v[50:51] op_sel:[1,0] op_sel_hi:[0,1]
	v_add_f32_e32 v30, v50, v51
	v_and_b32_e32 v51, 0xffff0000, v38
	v_and_b32_e32 v50, 0xffff0000, v34
	v_sub_f32_e32 v26, v52, v53
	v_pk_mul_f32 v[52:53], v[50:51], v[46:47]
	v_pk_mul_f32 v[46:47], v[46:47], v[50:51] op_sel:[1,0] op_sel_hi:[0,1]
	v_mul_f32_e32 v26, 0x3db504f3, v26
	v_mul_f32_e32 v30, 0x3db504f3, v30
	v_add_f32_e32 v46, v46, v47
	v_sub_f32_e32 v52, v52, v53
	v_cvt_pk_bf16_f32 v38, v56, v26
	v_cvt_pk_bf16_f32 v34, v57, v30
	v_cvt_pk_bf16_f32 v30, v54, v52
	v_cvt_pk_bf16_f32 v26, v55, v46
	v_lshlrev_b32_e32 v46, 16, v48
	v_and_b32_e32 v47, 0xffff0000, v48
	v_lshlrev_b32_e32 v51, 16, v31
	v_lshlrev_b32_e32 v50, 16, v27
	v_pk_mul_f32 v[52:53], v[50:51], v[46:47]
	v_pk_mul_f32 v[50:51], v[46:47], v[50:51] op_sel:[1,0] op_sel_hi:[0,1]
	v_sub_f32_e32 v48, v52, v53
	v_mul_f32_e32 v54, 0x3db504f3, v48
	v_add_f32_e32 v48, v50, v51
	v_lshlrev_b32_e32 v51, 16, v39
	v_lshlrev_b32_e32 v50, 16, v35
	v_pk_mul_f32 v[52:53], v[50:51], v[46:47]
	v_pk_mul_f32 v[46:47], v[46:47], v[50:51] op_sel:[1,0] op_sel_hi:[0,1]
	v_mul_f32_e32 v55, 0x3db504f3, v48
	v_sub_f32_e32 v52, v52, v53
	v_add_f32_e32 v53, v46, v47
	v_lshlrev_b32_e32 v46, 16, v49
	v_and_b32_e32 v47, 0xffff0000, v49
	v_and_b32_e32 v49, 0xffff0000, v31
	v_and_b32_e32 v48, 0xffff0000, v27
	v_pk_mul_f32 v[50:51], v[48:49], v[46:47]
	v_pk_mul_f32 v[48:49], v[46:47], v[48:49] op_sel:[1,0] op_sel_hi:[0,1]
	v_add_f32_e32 v31, v48, v49
	v_and_b32_e32 v49, 0xffff0000, v39
	v_and_b32_e32 v48, 0xffff0000, v35
	v_sub_f32_e32 v27, v50, v51
	v_pk_mul_f32 v[50:51], v[48:49], v[46:47]
	v_pk_mul_f32 v[46:47], v[46:47], v[48:49] op_sel:[1,0] op_sel_hi:[0,1]
	v_mul_f32_e32 v27, 0x3db504f3, v27
	v_mul_f32_e32 v31, 0x3db504f3, v31
	v_add_f32_e32 v46, v46, v47
	v_sub_f32_e32 v50, v50, v51
	v_cvt_pk_bf16_f32 v39, v54, v27
	v_cvt_pk_bf16_f32 v35, v55, v31
	v_cvt_pk_bf16_f32 v31, v52, v50
	v_cvt_pk_bf16_f32 v27, v53, v46
	v_lshlrev_b32_e32 v46, 16, v42
	v_and_b32_e32 v47, 0xffff0000, v42
	v_lshlrev_b32_e32 v49, 16, v32
	v_lshlrev_b32_e32 v48, 16, v28
	v_pk_mul_f32 v[50:51], v[48:49], v[46:47]
	v_pk_mul_f32 v[48:49], v[46:47], v[48:49] op_sel:[1,0] op_sel_hi:[0,1]
	v_sub_f32_e32 v42, v50, v51
	v_mul_f32_e32 v52, 0x3db504f3, v42
	v_add_f32_e32 v42, v48, v49
	v_lshlrev_b32_e32 v49, 16, v40
	v_lshlrev_b32_e32 v48, 16, v36
	v_pk_mul_f32 v[50:51], v[48:49], v[46:47]
	v_pk_mul_f32 v[46:47], v[46:47], v[48:49] op_sel:[1,0] op_sel_hi:[0,1]
	v_mul_f32_e32 v53, 0x3db504f3, v42
	v_sub_f32_e32 v50, v50, v51
	v_add_f32_e32 v51, v46, v47
	v_lshlrev_b32_e32 v42, 16, v43
	v_and_b32_e32 v43, 0xffff0000, v43
	v_and_b32_e32 v47, 0xffff0000, v32
	v_and_b32_e32 v46, 0xffff0000, v28
	v_pk_mul_f32 v[48:49], v[46:47], v[42:43]
	v_pk_mul_f32 v[46:47], v[42:43], v[46:47] op_sel:[1,0] op_sel_hi:[0,1]
	v_add_f32_e32 v32, v46, v47
	v_and_b32_e32 v47, 0xffff0000, v40
	v_and_b32_e32 v46, 0xffff0000, v36
	v_sub_f32_e32 v28, v48, v49
	v_pk_mul_f32 v[48:49], v[46:47], v[42:43]
	v_pk_mul_f32 v[42:43], v[42:43], v[46:47] op_sel:[1,0] op_sel_hi:[0,1]
	v_mul_f32_e32 v28, 0x3db504f3, v28
	v_mul_f32_e32 v32, 0x3db504f3, v32
	v_add_f32_e32 v42, v42, v43
	v_sub_f32_e32 v48, v48, v49
	v_cvt_pk_bf16_f32 v40, v52, v28
	v_cvt_pk_bf16_f32 v36, v53, v32
	v_cvt_pk_bf16_f32 v32, v50, v48
	v_cvt_pk_bf16_f32 v28, v51, v42
	v_and_b32_e32 v42, 0xffff0000, v44
	v_lshlrev_b32_e32 v43, 16, v44
	v_lshlrev_b32_e32 v47, 16, v41
	v_lshlrev_b32_e32 v46, 16, v37
	v_pk_mul_f32 v[48:49], v[46:47], v[42:43]
	v_pk_mul_f32 v[46:47], v[42:43], v[46:47] op_sel:[1,0] op_sel_hi:[0,1]
	v_add_f32_e32 v48, v48, v49
	v_sub_f32_e32 v49, v46, v47
	v_lshlrev_b32_e32 v47, 16, v33
	v_lshlrev_b32_e32 v46, 16, v29
	v_pk_mul_f32 v[50:51], v[46:47], v[42:43]
	v_pk_mul_f32 v[42:43], v[42:43], v[46:47] op_sel:[1,0] op_sel_hi:[0,1]
	v_add_f32_e32 v44, v50, v51
	v_mul_f32_e32 v50, 0x3db504f3, v44
	v_and_b32_e32 v44, 0xffff0000, v45
	v_lshlrev_b32_e32 v45, 16, v45
	v_and_b32_e32 v47, 0xffff0000, v33
	v_and_b32_e32 v46, 0xffff0000, v29
	v_sub_f32_e32 v42, v42, v43
	v_pk_mul_f32 v[52:53], v[44:45], v[46:47] op_sel:[1,0] op_sel_hi:[0,1]
	v_pk_mul_f32 v[46:47], v[46:47], v[44:45]
	v_mul_f32_e32 v51, 0x3db504f3, v42
	v_and_b32_e32 v43, 0xffff0000, v41
	v_and_b32_e32 v42, 0xffff0000, v37
	v_sub_f32_e32 v29, v52, v53
	v_add_f32_e32 v33, v46, v47
	v_mul_f32_e32 v29, 0x3db504f3, v29
	v_mul_f32_e32 v33, 0x3db504f3, v33
	v_pk_mul_f32 v[46:47], v[44:45], v[42:43] op_sel:[1,0] op_sel_hi:[0,1]
	v_pk_mul_f32 v[42:43], v[42:43], v[44:45]
	v_cvt_pk_bf16_f32 v41, v51, v29
	v_sub_f32_e32 v46, v46, v47
	v_add_f32_e32 v42, v42, v43
	v_cvt_pk_bf16_f32 v37, v50, v33
	v_cvt_pk_bf16_f32 v33, v49, v46
	v_cvt_pk_bf16_f32 v29, v48, v42
	ds_write_b128 v161, v[38:41] offset:16
	ds_write_b128 v161, v[34:37] offset:144
	ds_write_b128 v161, v[30:33] offset:34832
	ds_write_b128 v161, v[26:29] offset:34960
	s_cbranch_scc1 .LBB0_314
	s_add_i32 s93, s93, s3
	s_cmpk_lt_i32 s93, 0x80
	s_waitcnt lgkmcnt(0)
	s_barrier
	s_cbranch_scc1 .LBB0_311
